# v24 + attention softmax block: v_pk_fma_f32 for the exponent arguments (same fma per element) and v_pk_add_f32 pair row sums, second half in place (173 -> 142 instructions per key block)
# baseline (speedup 1.0000x reference)
.LBB0_527:
	s_mov_b32 s8, 0x3e0293ee
	v_lshrrev_b32_e32 v176, v171, v176
	v_pk_fma_f32 v[84:85], v[84:85], s[8:9], v[2:3] op_sel_hi:[1,0,0] neg_lo:[0,0,1] neg_hi:[0,0,1]
	v_pk_fma_f32 v[86:87], v[86:87], s[8:9], v[2:3] op_sel_hi:[1,0,0] neg_lo:[0,0,1] neg_hi:[0,0,1]
	v_exp_f32_e32 v84, v84
	v_bfe_i32 v250, v176, 0, 1
	v_exp_f32_e32 v85, v85
	v_bfe_i32 v251, v176, 1, 1
	v_and_b32_e32 v84, v84, v250
	v_and_b32_e32 v85, v85, v251
	v_pk_fma_f32 v[88:89], v[88:89], s[8:9], v[2:3] op_sel_hi:[1,0,0] neg_lo:[0,0,1] neg_hi:[0,0,1]
	v_exp_f32_e32 v86, v86
	v_bfe_i32 v250, v176, 2, 1
	v_exp_f32_e32 v87, v87
	v_bfe_i32 v251, v176, 3, 1
	v_and_b32_e32 v86, v86, v250
	v_and_b32_e32 v87, v87, v251
	v_pk_fma_f32 v[90:91], v[90:91], s[8:9], v[2:3] op_sel_hi:[1,0,0] neg_lo:[0,0,1] neg_hi:[0,0,1]
	v_exp_f32_e32 v88, v88
	v_bfe_i32 v250, v176, 8, 1
	v_exp_f32_e32 v89, v89
	v_bfe_i32 v251, v176, 9, 1
	v_and_b32_e32 v88, v88, v250
	v_pk_add_f32 v[252:253], v[84:85], v[86:87]
	v_and_b32_e32 v89, v89, v251
	v_pk_fma_f32 v[92:93], v[92:93], s[8:9], v[2:3] op_sel_hi:[1,0,0] neg_lo:[0,0,1] neg_hi:[0,0,1]
	v_exp_f32_e32 v90, v90
	v_bfe_i32 v250, v176, 10, 1
	v_exp_f32_e32 v91, v91
	v_bfe_i32 v251, v176, 11, 1
	v_and_b32_e32 v90, v90, v250
	v_pk_add_f32 v[252:253], v[88:89], v[252:253]
	v_and_b32_e32 v91, v91, v251
	v_pk_fma_f32 v[94:95], v[94:95], s[8:9], v[2:3] op_sel_hi:[1,0,0] neg_lo:[0,0,1] neg_hi:[0,0,1]
	v_exp_f32_e32 v92, v92
	v_bfe_i32 v250, v176, 16, 1
	v_exp_f32_e32 v93, v93
	v_bfe_i32 v251, v176, 17, 1
	v_and_b32_e32 v92, v92, v250
	v_pk_add_f32 v[252:253], v[90:91], v[252:253]
	v_and_b32_e32 v93, v93, v251
	v_pk_fma_f32 v[96:97], v[96:97], s[8:9], v[2:3] op_sel_hi:[1,0,0] neg_lo:[0,0,1] neg_hi:[0,0,1]
	v_exp_f32_e32 v94, v94
	v_bfe_i32 v250, v176, 18, 1
	v_exp_f32_e32 v95, v95
	v_bfe_i32 v251, v176, 19, 1
	v_and_b32_e32 v94, v94, v250
	v_pk_add_f32 v[252:253], v[92:93], v[252:253]
	v_and_b32_e32 v95, v95, v251
	v_pk_fma_f32 v[98:99], v[98:99], s[8:9], v[2:3] op_sel_hi:[1,0,0] neg_lo:[0,0,1] neg_hi:[0,0,1]
	v_exp_f32_e32 v96, v96
	v_bfe_i32 v250, v176, 24, 1
	v_exp_f32_e32 v97, v97
	v_bfe_i32 v251, v176, 25, 1
	v_and_b32_e32 v96, v96, v250
	v_pk_add_f32 v[252:253], v[94:95], v[252:253]
	v_and_b32_e32 v97, v97, v251
	v_lshrrev_b32_e32 v177, v171, v177
	v_pk_fma_f32 v[68:69], v[68:69], s[8:9], v[2:3] op_sel_hi:[1,0,0] neg_lo:[0,0,1] neg_hi:[0,0,1]
	v_exp_f32_e32 v98, v98
	v_bfe_i32 v250, v176, 26, 1
	v_exp_f32_e32 v99, v99
	v_bfe_i32 v251, v176, 27, 1
	v_and_b32_e32 v98, v98, v250
	v_pk_add_f32 v[252:253], v[96:97], v[252:253]
	v_and_b32_e32 v99, v99, v251
	s_mulk_i32 s7, 0x5000
	v_pk_fma_f32 v[70:71], v[70:71], s[8:9], v[2:3] op_sel_hi:[1,0,0] neg_lo:[0,0,1] neg_hi:[0,0,1]
	v_exp_f32_e32 v68, v68
	v_bfe_i32 v250, v177, 0, 1
	v_exp_f32_e32 v69, v69
	v_bfe_i32 v251, v177, 1, 1
	v_and_b32_e32 v185, v68, v250
	v_pk_add_f32 v[252:253], v[98:99], v[252:253]
	v_and_b32_e32 v186, v69, v251
	v_pk_fma_f32 v[72:73], v[72:73], s[8:9], v[2:3] op_sel_hi:[1,0,0] neg_lo:[0,0,1] neg_hi:[0,0,1]
	v_exp_f32_e32 v70, v70
	v_bfe_i32 v250, v177, 2, 1
	v_exp_f32_e32 v71, v71
	v_bfe_i32 v251, v177, 3, 1
	v_and_b32_e32 v187, v70, v250
	v_add_f32_e32 v252, v185, v252
	v_and_b32_e32 v188, v71, v251
	v_pk_fma_f32 v[74:75], v[74:75], s[8:9], v[2:3] op_sel_hi:[1,0,0] neg_lo:[0,0,1] neg_hi:[0,0,1]
	v_exp_f32_e32 v72, v72
	v_bfe_i32 v250, v177, 8, 1
	v_exp_f32_e32 v73, v73
	v_bfe_i32 v251, v177, 9, 1
	v_and_b32_e32 v189, v72, v250
	v_pk_add_f32 v[252:253], v[186:187], v[252:253]
	v_and_b32_e32 v190, v73, v251
	v_pk_fma_f32 v[76:77], v[76:77], s[8:9], v[2:3] op_sel_hi:[1,0,0] neg_lo:[0,0,1] neg_hi:[0,0,1]
	v_exp_f32_e32 v74, v74
	v_bfe_i32 v250, v177, 10, 1
	v_exp_f32_e32 v75, v75
	v_bfe_i32 v251, v177, 11, 1
	v_and_b32_e32 v191, v74, v250
	v_pk_add_f32 v[252:253], v[188:189], v[252:253]
	v_and_b32_e32 v192, v75, v251
	v_pk_fma_f32 v[78:79], v[78:79], s[8:9], v[2:3] op_sel_hi:[1,0,0] neg_lo:[0,0,1] neg_hi:[0,0,1]
	v_exp_f32_e32 v76, v76
	v_bfe_i32 v250, v177, 16, 1
	v_exp_f32_e32 v77, v77
	v_bfe_i32 v251, v177, 17, 1
	v_and_b32_e32 v193, v76, v250
	v_pk_add_f32 v[252:253], v[190:191], v[252:253]
	v_and_b32_e32 v194, v77, v251
	v_pk_fma_f32 v[80:81], v[80:81], s[8:9], v[2:3] op_sel_hi:[1,0,0] neg_lo:[0,0,1] neg_hi:[0,0,1]
	v_exp_f32_e32 v78, v78
	v_bfe_i32 v250, v177, 18, 1
	v_exp_f32_e32 v79, v79
	v_bfe_i32 v251, v177, 19, 1
	v_and_b32_e32 v195, v78, v250
	v_pk_add_f32 v[252:253], v[192:193], v[252:253]
	v_and_b32_e32 v196, v79, v251
	v_pk_fma_f32 v[82:83], v[82:83], s[8:9], v[2:3] op_sel_hi:[1,0,0] neg_lo:[0,0,1] neg_hi:[0,0,1]
	v_exp_f32_e32 v80, v80
	v_bfe_i32 v250, v177, 24, 1
	v_exp_f32_e32 v81, v81
	v_bfe_i32 v251, v177, 25, 1
	v_and_b32_e32 v197, v80, v250
	v_pk_add_f32 v[252:253], v[194:195], v[252:253]
	v_and_b32_e32 v198, v81, v251
	v_exp_f32_e32 v82, v82
	v_bfe_i32 v250, v177, 26, 1
	v_exp_f32_e32 v83, v83
	v_bfe_i32 v251, v177, 27, 1
	v_and_b32_e32 v199, v82, v250
	v_pk_add_f32 v[252:253], v[196:197], v[252:253]
	v_and_b32_e32 v2, v83, v251
	v_add_u32_e32 v177, s7, v180
	ds_read_b64_tr_b16 v[68:69], v177 offset:34816
	ds_read_b64_tr_b16 v[72:73], v177 offset:34880
	ds_read_b64_tr_b16 v[76:77], v177 offset:34944
	ds_read_b64_tr_b16 v[80:81], v177 offset:35008
	ds_read_b64_tr_b16 v[70:71], v177 offset:37376
	ds_read_b64_tr_b16 v[74:75], v177 offset:37440
	ds_read_b64_tr_b16 v[78:79], v177 offset:37504
	ds_read_b64_tr_b16 v[82:83], v177 offset:37568
	v_pk_add_f32 v[252:253], v[198:199], v[252:253]
	v_add_f32_e32 v253, v2, v253
	v_add_f32_e32 v176, v252, v253
	v_cvt_pk_bf16_f32 v84, v84, v85
	v_cvt_pk_bf16_f32 v85, v86, v87
	v_cvt_pk_bf16_f32 v86, v88, v89
	v_cvt_pk_bf16_f32 v87, v90, v91
	s_waitcnt lgkmcnt(3)
	s_nop 0
	v_mfma_f32_32x32x16_bf16 v[52:67], v[68:71], v[84:87], v[52:67]
	s_waitcnt lgkmcnt(2)
	v_mfma_f32_32x32x16_bf16 v[36:51], v[72:75], v[84:87], v[36:51]
	s_waitcnt lgkmcnt(1)
	v_mfma_f32_32x32x16_bf16 v[20:35], v[76:79], v[84:87], v[20:35]
	ds_read_b64_tr_b16 v[68:69], v177 offset:39936
	ds_read_b64_tr_b16 v[72:73], v177 offset:40000
	ds_read_b64_tr_b16 v[76:77], v177 offset:40064
	ds_read_b64_tr_b16 v[88:89], v177 offset:40128
	ds_read_b64_tr_b16 v[70:71], v177 offset:42496
	ds_read_b64_tr_b16 v[74:75], v177 offset:42560
	ds_read_b64_tr_b16 v[78:79], v177 offset:42624
	ds_read_b64_tr_b16 v[90:91], v177 offset:42688
	s_waitcnt lgkmcnt(8)
	v_mfma_f32_32x32x16_bf16 v[4:19], v[80:83], v[84:87], v[4:19]
	v_cvt_pk_bf16_f32 v80, v92, v93
	v_cvt_pk_bf16_f32 v81, v94, v95
	v_cvt_pk_bf16_f32 v82, v96, v97
	v_cvt_pk_bf16_f32 v83, v98, v99
	s_waitcnt lgkmcnt(3)
	s_nop 0
	v_mfma_f32_32x32x16_bf16 v[52:67], v[68:71], v[80:83], v[52:67]
	s_waitcnt lgkmcnt(2)
	v_mfma_f32_32x32x16_bf16 v[36:51], v[72:75], v[80:83], v[36:51]
	s_waitcnt lgkmcnt(1)
	v_mfma_f32_32x32x16_bf16 v[20:35], v[76:79], v[80:83], v[20:35]
	ds_read_b64_tr_b16 v[68:69], v177 offset:45056
	ds_read_b64_tr_b16 v[72:73], v177 offset:45120
	ds_read_b64_tr_b16 v[76:77], v177 offset:45184
	ds_read_b64_tr_b16 v[84:85], v177 offset:45248
	ds_read_b64_tr_b16 v[70:71], v177 offset:47616
	ds_read_b64_tr_b16 v[74:75], v177 offset:47680
	ds_read_b64_tr_b16 v[78:79], v177 offset:47744
	ds_read_b64_tr_b16 v[86:87], v177 offset:47808
	s_waitcnt lgkmcnt(8)
	v_mfma_f32_32x32x16_bf16 v[4:19], v[88:91], v[80:83], v[4:19]
	v_cvt_pk_bf16_f32 v80, v185, v186
	v_cvt_pk_bf16_f32 v81, v187, v188
	v_cvt_pk_bf16_f32 v82, v189, v190
	v_cvt_pk_bf16_f32 v83, v191, v192
	s_waitcnt lgkmcnt(3)
	s_nop 0
	v_mfma_f32_32x32x16_bf16 v[52:67], v[68:71], v[80:83], v[52:67]
	s_waitcnt lgkmcnt(2)
	v_mfma_f32_32x32x16_bf16 v[36:51], v[72:75], v[80:83], v[36:51]
	s_waitcnt lgkmcnt(1)
	v_mfma_f32_32x32x16_bf16 v[20:35], v[76:79], v[80:83], v[20:35]
	ds_read_b64_tr_b16 v[68:69], v177 offset:50176
	ds_read_b64_tr_b16 v[72:73], v177 offset:50240
	ds_read_b64_tr_b16 v[76:77], v177 offset:50304
	ds_read_b64_tr_b16 v[88:89], v177 offset:50368
	ds_read_b64_tr_b16 v[70:71], v177 offset:52736
	ds_read_b64_tr_b16 v[74:75], v177 offset:52800
	ds_read_b64_tr_b16 v[78:79], v177 offset:52864
	ds_read_b64_tr_b16 v[90:91], v177 offset:52928
	s_waitcnt lgkmcnt(8)
	v_mfma_f32_32x32x16_bf16 v[4:19], v[84:87], v[80:83], v[4:19]
	v_cvt_pk_bf16_f32 v80, v193, v194
	v_cvt_pk_bf16_f32 v81, v195, v196
	v_cvt_pk_bf16_f32 v82, v197, v198
	v_cvt_pk_bf16_f32 v83, v199, v2
	v_add_f32_e32 v183, v183, v176
	s_waitcnt lgkmcnt(3)
	v_mfma_f32_32x32x16_bf16 v[52:67], v[68:71], v[80:83], v[52:67]
	s_waitcnt lgkmcnt(2)
	v_mfma_f32_32x32x16_bf16 v[36:51], v[72:75], v[80:83], v[36:51]
	s_waitcnt lgkmcnt(1)
	v_mfma_f32_32x32x16_bf16 v[20:35], v[76:79], v[80:83], v[20:35]
	s_waitcnt lgkmcnt(0)
	v_mfma_f32_32x32x16_bf16 v[4:19], v[88:91], v[80:83], v[4:19]
